# fp8 GEMM loops: no per-unit accumulator zeroing (first K step MFMAs take SrcC=0)
# baseline (speedup 1.0000x reference)
.LBB0_459:
	s_and_b64 s[46:47], s[38:39], exec
	s_cselect_b32 s48, s35, s43
	s_cselect_b32 s49, s34, s42
	s_cselect_b32 s66, s37, s45
	s_cselect_b32 s67, s36, s44
	s_add_u32 s42, s42, 0x80
	s_addc_u32 s43, s43, 0
	s_add_u32 s68, s44, 0x100
	s_mov_b32 s101, 0
	s_addc_u32 s69, s45, 0
	s_mov_b32 s70, -2
.LBB0_460:
	ds_read_b128 v[18:21], v194
	ds_read_b128 v[22:25], v194 offset:1024
	ds_read_b128 v[26:29], v194 offset:2048
	ds_read_b128 v[30:33], v194 offset:3072
	ds_read_b128 v[2:5], v195
	ds_read_b128 v[6:9], v195 offset:1024
	ds_read_b128 v[10:13], v195 offset:2048
	ds_read_b128 v[14:17], v195 offset:3072
	s_add_u32 s44, s42, 0x80
	s_addc_u32 s45, s43, 0
	s_cmp_eq_u32 s70, 12
	s_cselect_b32 s47, s48, s45
	s_cselect_b32 s46, s49, s44
	s_cselect_b32 s45, s66, s69
	s_cselect_b32 s44, s67, s68
	v_lshl_add_u64 v[222:223], s[42:43], 0, v[180:181]
	s_add_i32 m0, s41, 0xc000
	ds_read_b128 v[184:187], v196
	ds_read_b128 v[188:191], v196 offset:1024
	ds_read_b128 v[198:201], v196 offset:2048
	ds_read_b128 v[202:205], v196 offset:3072
	ds_read_b128 v[206:209], v196 offset:4096
	ds_read_b128 v[210:213], v196 offset:5120
	ds_read_b128 v[214:217], v196 offset:6144
	ds_read_b128 v[218:221], v196 offset:7168
	global_load_lds_dwordx4 v[222:223], off
	v_lshl_add_u64 v[222:223], s[42:43], 0, v[178:179]
	s_add_i32 m0, s41, 0xe000
	s_nop 0
	global_load_lds_dwordx4 v[222:223], off
	s_waitcnt vmcnt(8)
	s_waitcnt lgkmcnt(0)
	s_barrier
	s_setprio 1
	s_waitcnt lgkmcnt(0)
	s_cmp_eq_u32 s101, 0
	s_cbranch_scc1 .Lmy_z_p1b_0
	s_nop 1
	v_mfma_f32_16x16x128_f8f6f4 v[158:161], v[18:25], v[184:191], v[158:161]
	v_mfma_f32_16x16x128_f8f6f4 v[154:157], v[26:33], v[184:191], v[154:157]
	v_mfma_f32_16x16x128_f8f6f4 v[142:145], v[18:25], v[198:205], v[142:145]
	v_mfma_f32_16x16x128_f8f6f4 v[138:141], v[26:33], v[198:205], v[138:141]
	v_mfma_f32_16x16x128_f8f6f4 v[126:129], v[18:25], v[206:213], v[126:129]
	v_mfma_f32_16x16x128_f8f6f4 v[122:125], v[26:33], v[206:213], v[122:125]
	v_mfma_f32_16x16x128_f8f6f4 v[110:113], v[18:25], v[214:221], v[110:113]
	v_mfma_f32_16x16x128_f8f6f4 v[106:109], v[26:33], v[214:221], v[106:109]
	s_branch .Lmy_zd_p1b_0
.Lmy_z_p1b_0:
	s_nop 1
	v_mfma_f32_16x16x128_f8f6f4 v[158:161], v[18:25], v[184:191], 0
	v_mfma_f32_16x16x128_f8f6f4 v[154:157], v[26:33], v[184:191], 0
	v_mfma_f32_16x16x128_f8f6f4 v[142:145], v[18:25], v[198:205], 0
	v_mfma_f32_16x16x128_f8f6f4 v[138:141], v[26:33], v[198:205], 0
	v_mfma_f32_16x16x128_f8f6f4 v[126:129], v[18:25], v[206:213], 0
	v_mfma_f32_16x16x128_f8f6f4 v[122:125], v[26:33], v[206:213], 0
	v_mfma_f32_16x16x128_f8f6f4 v[110:113], v[18:25], v[214:221], 0
	v_mfma_f32_16x16x128_f8f6f4 v[106:109], v[26:33], v[214:221], 0
.Lmy_zd_p1b_0:
	s_setprio 0
	s_setprio 1
	s_cmp_eq_u32 s101, 0
	s_cbranch_scc1 .Lmy_z_p1b_1
	s_nop 1
	v_mfma_f32_16x16x128_f8f6f4 v[150:153], v[2:9], v[184:191], v[150:153]
	v_mfma_f32_16x16x128_f8f6f4 v[146:149], v[10:17], v[184:191], v[146:149]
	v_mfma_f32_16x16x128_f8f6f4 v[134:137], v[2:9], v[198:205], v[134:137]
	v_mfma_f32_16x16x128_f8f6f4 v[130:133], v[10:17], v[198:205], v[130:133]
	v_mfma_f32_16x16x128_f8f6f4 v[118:121], v[2:9], v[206:213], v[118:121]
	v_mfma_f32_16x16x128_f8f6f4 v[114:117], v[10:17], v[206:213], v[114:117]
	v_mfma_f32_16x16x128_f8f6f4 v[102:105], v[2:9], v[214:221], v[102:105]
	v_mfma_f32_16x16x128_f8f6f4 v[98:101], v[10:17], v[214:221], v[98:101]
	s_branch .Lmy_zd_p1b_1
.Lmy_z_p1b_1:
	s_nop 1
	v_mfma_f32_16x16x128_f8f6f4 v[150:153], v[2:9], v[184:191], 0
	v_mfma_f32_16x16x128_f8f6f4 v[146:149], v[10:17], v[184:191], 0
	v_mfma_f32_16x16x128_f8f6f4 v[134:137], v[2:9], v[198:205], 0
	v_mfma_f32_16x16x128_f8f6f4 v[130:133], v[10:17], v[198:205], 0
	v_mfma_f32_16x16x128_f8f6f4 v[118:121], v[2:9], v[206:213], 0
	v_mfma_f32_16x16x128_f8f6f4 v[114:117], v[10:17], v[206:213], 0
	v_mfma_f32_16x16x128_f8f6f4 v[102:105], v[2:9], v[214:221], 0
	v_mfma_f32_16x16x128_f8f6f4 v[98:101], v[10:17], v[214:221], 0
.Lmy_zd_p1b_1:
	s_setprio 0
	s_barrier
	s_add_i32 s71, s61, s53
	v_lshl_add_u64 v[184:185], s[44:45], 0, v[162:163]
	s_mov_b32 m0, s71
	ds_read_b128 v[198:201], v196 offset:16384
	ds_read_b128 v[202:205], v196 offset:17408
	ds_read_b128 v[206:209], v196 offset:18432
	ds_read_b128 v[210:213], v196 offset:19456
	ds_read_b128 v[214:217], v196 offset:20480
	ds_read_b128 v[218:221], v196 offset:21504
	ds_read_b128 v[230:233], v196 offset:22528
	ds_read_b128 v[234:237], v196 offset:23552
	global_load_lds_dwordx4 v[184:185], off
	s_add_i32 m0, s71, 0x2000
	s_add_u32 s72, s44, 0x40000
	v_lshl_add_u64 v[186:187], s[44:45], 0, v[164:165]
	s_addc_u32 s73, s45, 0
	s_add_i32 s71, s62, s53
	global_load_lds_dwordx4 v[186:187], off
	v_lshl_add_u64 v[188:189], s[72:73], 0, v[162:163]
	s_mov_b32 m0, s71
	v_lshl_add_u64 v[190:191], s[46:47], 0, v[168:169]
	global_load_lds_dwordx4 v[188:189], off
	v_lshl_add_u64 v[188:189], s[72:73], 0, v[164:165]
	s_add_i32 m0, s71, 0x2000
	s_nop 0
	global_load_lds_dwordx4 v[188:189], off
	v_lshl_add_u64 v[188:189], s[46:47], 0, v[166:167]
	s_mov_b32 m0, s41
	s_nop 0
	global_load_lds_dwordx4 v[188:189], off
	s_mov_b32 m0, s54
	s_nop 0
	global_load_lds_dwordx4 v[190:191], off
	s_waitcnt vmcnt(8)
	s_waitcnt lgkmcnt(0)
	s_barrier
	s_setprio 1
	s_waitcnt lgkmcnt(0)
	s_cmp_eq_u32 s101, 0
	s_cbranch_scc1 .Lmy_z_p1b_2
	s_nop 1
	v_mfma_f32_16x16x128_f8f6f4 v[90:93], v[18:25], v[198:205], v[90:93]
	v_mfma_f32_16x16x128_f8f6f4 v[82:85], v[26:33], v[198:205], v[82:85]
	v_mfma_f32_16x16x128_f8f6f4 v[70:73], v[18:25], v[206:213], v[70:73]
	v_mfma_f32_16x16x128_f8f6f4 v[66:69], v[26:33], v[206:213], v[66:69]
	v_mfma_f32_16x16x128_f8f6f4 v[54:57], v[18:25], v[214:221], v[54:57]
	v_mfma_f32_16x16x128_f8f6f4 v[50:53], v[26:33], v[214:221], v[50:53]
	v_mfma_f32_16x16x128_f8f6f4 v[38:41], v[18:25], v[230:237], v[38:41]
	v_mfma_f32_16x16x128_f8f6f4 v[34:37], v[26:33], v[230:237], v[34:37]
	s_branch .Lmy_zd_p1b_2
.Lmy_z_p1b_2:
	s_nop 1
	v_mfma_f32_16x16x128_f8f6f4 v[90:93], v[18:25], v[198:205], 0
	v_mfma_f32_16x16x128_f8f6f4 v[82:85], v[26:33], v[198:205], 0
	v_mfma_f32_16x16x128_f8f6f4 v[70:73], v[18:25], v[206:213], 0
	v_mfma_f32_16x16x128_f8f6f4 v[66:69], v[26:33], v[206:213], 0
	v_mfma_f32_16x16x128_f8f6f4 v[54:57], v[18:25], v[214:221], 0
	v_mfma_f32_16x16x128_f8f6f4 v[50:53], v[26:33], v[214:221], 0
	v_mfma_f32_16x16x128_f8f6f4 v[38:41], v[18:25], v[230:237], 0
	v_mfma_f32_16x16x128_f8f6f4 v[34:37], v[26:33], v[230:237], 0
.Lmy_zd_p1b_2:
	s_setprio 0
	s_setprio 1
	s_cmp_eq_u32 s101, 0
	s_cbranch_scc1 .Lmy_z_p1b_3
	s_nop 1
	v_mfma_f32_16x16x128_f8f6f4 v[94:97], v[2:9], v[198:205], v[94:97]
	v_mfma_f32_16x16x128_f8f6f4 v[86:89], v[10:17], v[198:205], v[86:89]
	v_mfma_f32_16x16x128_f8f6f4 v[78:81], v[2:9], v[206:213], v[78:81]
	v_mfma_f32_16x16x128_f8f6f4 v[74:77], v[10:17], v[206:213], v[74:77]
	v_mfma_f32_16x16x128_f8f6f4 v[62:65], v[2:9], v[214:221], v[62:65]
	v_mfma_f32_16x16x128_f8f6f4 v[58:61], v[10:17], v[214:221], v[58:61]
	v_mfma_f32_16x16x128_f8f6f4 v[46:49], v[2:9], v[230:237], v[46:49]
	v_mfma_f32_16x16x128_f8f6f4 v[42:45], v[10:17], v[230:237], v[42:45]
	s_branch .Lmy_zd_p1b_3
.Lmy_z_p1b_3:
	s_nop 1
	v_mfma_f32_16x16x128_f8f6f4 v[94:97], v[2:9], v[198:205], 0
	v_mfma_f32_16x16x128_f8f6f4 v[86:89], v[10:17], v[198:205], 0
	v_mfma_f32_16x16x128_f8f6f4 v[78:81], v[2:9], v[206:213], 0
	v_mfma_f32_16x16x128_f8f6f4 v[74:77], v[10:17], v[206:213], 0
	v_mfma_f32_16x16x128_f8f6f4 v[62:65], v[2:9], v[214:221], 0
	v_mfma_f32_16x16x128_f8f6f4 v[58:61], v[10:17], v[214:221], 0
	v_mfma_f32_16x16x128_f8f6f4 v[46:49], v[2:9], v[230:237], 0
	v_mfma_f32_16x16x128_f8f6f4 v[42:45], v[10:17], v[230:237], 0
.Lmy_zd_p1b_3:
	s_mov_b32 s101, 1
	s_setprio 0
	s_barrier
	s_add_i32 s71, 0, 0x18000
	s_add_i32 s72, 0, 0x1c000
	v_add_u32_e32 v14, s71, v192
	v_add_u32_e32 v30, s72, v192
	ds_read_b128 v[2:5], v14
	ds_read_b128 v[6:9], v14 offset:1024
	ds_read_b128 v[10:13], v14 offset:2048
	ds_read_b128 v[14:17], v14 offset:3072
	ds_read_b128 v[18:21], v30
	ds_read_b128 v[22:25], v30 offset:1024
	ds_read_b128 v[26:29], v30 offset:2048
	ds_read_b128 v[30:33], v30 offset:3072
	s_mov_b32 m0, s55
	v_lshl_add_u64 v[222:223], s[46:47], 0, v[170:171]
	ds_read_b128 v[198:201], v196 offset:32768
	ds_read_b128 v[202:205], v196 offset:33792
	ds_read_b128 v[206:209], v196 offset:34816
	ds_read_b128 v[210:213], v196 offset:35840
	ds_read_b128 v[214:217], v196 offset:36864
	ds_read_b128 v[218:221], v196 offset:37888
	ds_read_b128 v[230:233], v196 offset:38912
	ds_read_b128 v[234:237], v196 offset:39936
	global_load_lds_dwordx4 v[222:223], off
	v_lshl_add_u64 v[222:223], s[46:47], 0, v[172:173]
	s_mov_b32 m0, s58
	s_nop 0
	global_load_lds_dwordx4 v[222:223], off
	s_waitcnt vmcnt(8)
	s_waitcnt lgkmcnt(0)
	s_barrier
	s_setprio 1
	s_waitcnt lgkmcnt(0)
	s_nop 1
	v_mfma_f32_16x16x128_f8f6f4 v[158:161], v[2:9], v[198:205], v[158:161]
	v_mfma_f32_16x16x128_f8f6f4 v[154:157], v[10:17], v[198:205], v[154:157]
	v_mfma_f32_16x16x128_f8f6f4 v[142:145], v[2:9], v[206:213], v[142:145]
	v_mfma_f32_16x16x128_f8f6f4 v[138:141], v[10:17], v[206:213], v[138:141]
	v_mfma_f32_16x16x128_f8f6f4 v[126:129], v[2:9], v[214:221], v[126:129]
	v_mfma_f32_16x16x128_f8f6f4 v[122:125], v[10:17], v[214:221], v[122:125]
	v_mfma_f32_16x16x128_f8f6f4 v[110:113], v[2:9], v[230:237], v[110:113]
	v_mfma_f32_16x16x128_f8f6f4 v[106:109], v[10:17], v[230:237], v[106:109]
	s_setprio 0
	s_setprio 1
	s_nop 1
	v_mfma_f32_16x16x128_f8f6f4 v[150:153], v[18:25], v[198:205], v[150:153]
	v_mfma_f32_16x16x128_f8f6f4 v[146:149], v[26:33], v[198:205], v[146:149]
	v_mfma_f32_16x16x128_f8f6f4 v[134:137], v[18:25], v[206:213], v[134:137]
	v_mfma_f32_16x16x128_f8f6f4 v[130:133], v[26:33], v[206:213], v[130:133]
	v_mfma_f32_16x16x128_f8f6f4 v[118:121], v[18:25], v[214:221], v[118:121]
	v_mfma_f32_16x16x128_f8f6f4 v[114:117], v[26:33], v[214:221], v[114:117]
	v_mfma_f32_16x16x128_f8f6f4 v[102:105], v[18:25], v[230:237], v[102:105]
	v_mfma_f32_16x16x128_f8f6f4 v[98:101], v[26:33], v[230:237], v[98:101]
	s_setprio 0
	s_barrier
	s_add_i32 s46, s71, s53
	v_lshl_add_u64 v[184:185], v[184:185], 0, s[12:13]
	s_mov_b32 m0, s46
	ds_read_b128 v[198:201], v196 offset:49152
	ds_read_b128 v[202:205], v196 offset:50176
	ds_read_b128 v[206:209], v196 offset:51200
	ds_read_b128 v[210:213], v196 offset:52224
	ds_read_b128 v[214:217], v196 offset:53248
	ds_read_b128 v[218:221], v196 offset:54272
	ds_read_b128 v[230:233], v196 offset:55296
	ds_read_b128 v[234:237], v196 offset:56320
	global_load_lds_dwordx4 v[184:185], off
	s_add_i32 m0, s46, 0x2000
	s_add_u32 s44, s44, 0x40080
	v_lshl_add_u64 v[184:185], v[186:187], 0, s[12:13]
	s_addc_u32 s45, s45, 0
	s_add_i32 s46, s72, s53
	global_load_lds_dwordx4 v[184:185], off
	v_lshl_add_u64 v[184:185], s[44:45], 0, v[162:163]
	s_mov_b32 m0, s46
	s_nop 0
	global_load_lds_dwordx4 v[184:185], off
	v_lshl_add_u64 v[184:185], s[44:45], 0, v[164:165]
	s_add_i32 m0, s46, 0x2000
	s_nop 0
	global_load_lds_dwordx4 v[184:185], off
	v_lshl_add_u64 v[184:185], v[188:189], 0, s[12:13]
	s_mov_b32 m0, s59
	s_nop 0
	global_load_lds_dwordx4 v[184:185], off
	v_lshl_add_u64 v[184:185], v[190:191], 0, s[12:13]
	s_mov_b32 m0, s60
	s_nop 0
	global_load_lds_dwordx4 v[184:185], off
	s_waitcnt vmcnt(8)
	s_waitcnt lgkmcnt(0)
	s_barrier
	s_setprio 1
	s_waitcnt lgkmcnt(0)
	s_nop 1
	v_mfma_f32_16x16x128_f8f6f4 v[90:93], v[2:9], v[198:205], v[90:93]
	v_mfma_f32_16x16x128_f8f6f4 v[82:85], v[10:17], v[198:205], v[82:85]
	v_mfma_f32_16x16x128_f8f6f4 v[70:73], v[2:9], v[206:213], v[70:73]
	v_mfma_f32_16x16x128_f8f6f4 v[66:69], v[10:17], v[206:213], v[66:69]
	v_mfma_f32_16x16x128_f8f6f4 v[54:57], v[2:9], v[214:221], v[54:57]
	v_mfma_f32_16x16x128_f8f6f4 v[50:53], v[10:17], v[214:221], v[50:53]
	v_mfma_f32_16x16x128_f8f6f4 v[38:41], v[2:9], v[230:237], v[38:41]
	v_mfma_f32_16x16x128_f8f6f4 v[34:37], v[10:17], v[230:237], v[34:37]
	s_setprio 0
	s_setprio 1
	s_nop 1
	v_mfma_f32_16x16x128_f8f6f4 v[94:97], v[18:25], v[198:205], v[94:97]
	v_mfma_f32_16x16x128_f8f6f4 v[86:89], v[26:33], v[198:205], v[86:89]
	v_mfma_f32_16x16x128_f8f6f4 v[78:81], v[18:25], v[206:213], v[78:81]
	v_mfma_f32_16x16x128_f8f6f4 v[74:77], v[26:33], v[206:213], v[74:77]
	v_mfma_f32_16x16x128_f8f6f4 v[62:65], v[18:25], v[214:221], v[62:65]
	v_mfma_f32_16x16x128_f8f6f4 v[58:61], v[26:33], v[214:221], v[58:61]
	v_mfma_f32_16x16x128_f8f6f4 v[46:49], v[18:25], v[230:237], v[46:49]
	v_mfma_f32_16x16x128_f8f6f4 v[42:45], v[26:33], v[230:237], v[42:45]
	s_setprio 0
	s_barrier
	s_add_i32 s70, s70, 2
	s_add_u32 s42, s42, 0x100
	s_addc_u32 s43, s43, 0
	s_add_u32 s68, s68, 0x100
	s_addc_u32 s69, s69, 0
	s_cmp_gt_u32 s70, 13
	s_cbranch_scc0 .LBB0_460
	s_and_b64 vcc, exec, s[0:1]
	s_cbranch_vccz .LBB0_463
	s_barrier

.LBB0_1346:
	s_ashr_i32 s17, s16, 31
	s_lshl_b64 s[24:25], s[16:17], 16
	s_add_i32 s17, s50, 0x80
	v_add_u32_e32 v202, s17, v1
	v_add_u32_e32 v203, s17, v190
	s_lshl_b32 s17, s16, 2
	s_add_i32 s17, s17, 0
	s_add_i32 s17, s17, 0x20000
	s_add_u32 s24, s18, s24
	s_addc_u32 s25, s19, s25
	v_mov_b32_e32 v175, v167
	v_mov_b32_e32 v173, v167
	s_add_u32 s56, s26, 0x100
	s_mov_b32 s101, 0
	v_add_u32_e32 v200, s50, v1
	v_add_u32_e32 v201, s50, v190
	v_lshl_add_u64 v[178:179], s[10:11], 0, v[172:173]
	v_lshl_add_u64 v[180:181], s[10:11], 0, v[174:175]
	s_addc_u32 s57, s27, 0
	s_mov_b32 s58, -2
	s_mov_b64 s[26:27], 0
	s_xor_b64 s[28:29], s[22:23], -1
	v_mov_b32_e32 v169, v199
	v_mov_b32_e32 v171, v176
	v_mov_b32_e32 v173, v174
	v_mov_b32_e32 v175, v172
	s_branch .LBB0_1348
.LBB0_1347:
	s_add_u32 s30, s84, s26
	s_addc_u32 s31, s85, s27
	v_add_u32_e32 v2, s3, v193
	v_add_u32_e32 v14, s2, v193
	s_add_u32 s34, s30, 0x35400100
	ds_read_b128 v[18:21], v2
	ds_read_b128 v[22:25], v2 offset:1024
	ds_read_b128 v[26:29], v2 offset:2048
	ds_read_b128 v[30:33], v2 offset:3072
	ds_read_b128 v[2:5], v14
	ds_read_b128 v[6:9], v14 offset:1024
	ds_read_b128 v[10:13], v14 offset:2048
	ds_read_b128 v[14:17], v14 offset:3072
	s_addc_u32 s35, s31, 0
	s_add_u32 s59, s56, s26
	s_addc_u32 s60, s57, s27
	s_cmpk_eq_i32 s26, 0x700
	s_cselect_b64 vcc, -1, 0
	s_and_b64 s[30:31], vcc, exec
	v_cndmask_b32_e32 v166, v199, v169, vcc
	s_cselect_b32 s35, s5, s35
	s_cselect_b32 s34, s4, s34
	v_cndmask_b32_e32 v238, v176, v171, vcc
	v_cndmask_b32_e32 v229, v174, v173, vcc
	v_cndmask_b32_e32 v240, v172, v175, vcc
	s_cselect_b32 s31, s21, s60
	s_cselect_b32 s30, s20, s59
	v_lshl_add_u64 v[230:231], v[180:181], 0, s[26:27]
	s_add_i32 m0, s39, 0xc000
	ds_read_b128 v[182:185], v197
	ds_read_b128 v[186:189], v197 offset:1024
	ds_read_b128 v[204:207], v197 offset:2048
	ds_read_b128 v[208:211], v197 offset:3072
	ds_read_b128 v[212:215], v197 offset:4096
	ds_read_b128 v[216:219], v197 offset:5120
	ds_read_b128 v[220:223], v197 offset:6144
	ds_read_b128 v[224:227], v197 offset:7168
	global_load_lds_dwordx4 v[230:231], off
	v_lshl_add_u64 v[230:231], v[178:179], 0, s[26:27]
	s_add_i32 m0, s39, 0xe000
	s_nop 0
	global_load_lds_dwordx4 v[230:231], off
	s_waitcnt vmcnt(8)
	s_waitcnt lgkmcnt(0)
	s_barrier
	s_setprio 1
	s_waitcnt lgkmcnt(0)
	s_cmp_eq_u32 s101, 0
	s_cbranch_scc1 .Lmy_z_p8_0
	s_nop 1
	v_mfma_f32_16x16x128_f8f6f4 v[158:161], v[18:25], v[182:189], v[158:161]
	v_mfma_f32_16x16x128_f8f6f4 v[150:153], v[26:33], v[182:189], v[150:153]
	v_mfma_f32_16x16x128_f8f6f4 v[142:145], v[18:25], v[204:211], v[142:145]
	v_mfma_f32_16x16x128_f8f6f4 v[134:137], v[26:33], v[204:211], v[134:137]
	v_mfma_f32_16x16x128_f8f6f4 v[126:129], v[18:25], v[212:219], v[126:129]
	v_mfma_f32_16x16x128_f8f6f4 v[118:121], v[26:33], v[212:219], v[118:121]
	v_mfma_f32_16x16x128_f8f6f4 v[110:113], v[18:25], v[220:227], v[110:113]
	v_mfma_f32_16x16x128_f8f6f4 v[102:105], v[26:33], v[220:227], v[102:105]
	s_branch .Lmy_zd_p8_0
.Lmy_z_p8_0:
	s_nop 1
	v_mfma_f32_16x16x128_f8f6f4 v[158:161], v[18:25], v[182:189], 0
	v_mfma_f32_16x16x128_f8f6f4 v[150:153], v[26:33], v[182:189], 0
	v_mfma_f32_16x16x128_f8f6f4 v[142:145], v[18:25], v[204:211], 0
	v_mfma_f32_16x16x128_f8f6f4 v[134:137], v[26:33], v[204:211], 0
	v_mfma_f32_16x16x128_f8f6f4 v[126:129], v[18:25], v[212:219], 0
	v_mfma_f32_16x16x128_f8f6f4 v[118:121], v[26:33], v[212:219], 0
	v_mfma_f32_16x16x128_f8f6f4 v[110:113], v[18:25], v[220:227], 0
	v_mfma_f32_16x16x128_f8f6f4 v[102:105], v[26:33], v[220:227], 0
.Lmy_zd_p8_0:
	s_setprio 0
	s_setprio 1
	s_cmp_eq_u32 s101, 0
	s_cbranch_scc1 .Lmy_z_p8_1
	s_nop 1
	v_mfma_f32_16x16x128_f8f6f4 v[154:157], v[2:9], v[182:189], v[154:157]
	v_mfma_f32_16x16x128_f8f6f4 v[146:149], v[10:17], v[182:189], v[146:149]
	v_mfma_f32_16x16x128_f8f6f4 v[138:141], v[2:9], v[204:211], v[138:141]
	v_mfma_f32_16x16x128_f8f6f4 v[130:133], v[10:17], v[204:211], v[130:133]
	v_mfma_f32_16x16x128_f8f6f4 v[122:125], v[2:9], v[212:219], v[122:125]
	v_mfma_f32_16x16x128_f8f6f4 v[114:117], v[10:17], v[212:219], v[114:117]
	v_mfma_f32_16x16x128_f8f6f4 v[106:109], v[2:9], v[220:227], v[106:109]
	v_mfma_f32_16x16x128_f8f6f4 v[98:101], v[10:17], v[220:227], v[98:101]
	s_branch .Lmy_zd_p8_1
.Lmy_z_p8_1:
	s_nop 1
	v_mfma_f32_16x16x128_f8f6f4 v[154:157], v[2:9], v[182:189], 0
	v_mfma_f32_16x16x128_f8f6f4 v[146:149], v[10:17], v[182:189], 0
	v_mfma_f32_16x16x128_f8f6f4 v[138:141], v[2:9], v[204:211], 0
	v_mfma_f32_16x16x128_f8f6f4 v[130:133], v[10:17], v[204:211], 0
	v_mfma_f32_16x16x128_f8f6f4 v[122:125], v[2:9], v[212:219], 0
	v_mfma_f32_16x16x128_f8f6f4 v[114:117], v[10:17], v[212:219], 0
	v_mfma_f32_16x16x128_f8f6f4 v[106:109], v[2:9], v[220:227], 0
	v_mfma_f32_16x16x128_f8f6f4 v[98:101], v[10:17], v[220:227], 0
.Lmy_zd_p8_1:
	s_setprio 0
	s_barrier
	s_add_i32 s59, s3, s38
	v_lshl_add_u64 v[182:183], s[30:31], 0, v[164:165]
	s_mov_b32 m0, s59
	ds_read_b128 v[204:207], v197 offset:16384
	ds_read_b128 v[208:211], v197 offset:17408
	ds_read_b128 v[212:215], v197 offset:18432
	ds_read_b128 v[216:219], v197 offset:19456
	ds_read_b128 v[220:223], v197 offset:20480
	ds_read_b128 v[224:227], v197 offset:21504
	ds_read_b128 v[230:233], v197 offset:22528
	ds_read_b128 v[234:237], v197 offset:23552
	global_load_lds_dwordx4 v[182:183], off
	s_add_i32 m0, s59, 0x2000
	s_add_u32 s60, s30, 0x40000
	v_lshl_add_u64 v[184:185], s[30:31], 0, v[162:163]
	s_addc_u32 s61, s31, 0
	s_add_i32 s59, s2, s38
	global_load_lds_dwordx4 v[184:185], off
	v_lshl_add_u64 v[186:187], s[60:61], 0, v[164:165]
	s_mov_b32 m0, s59
	v_mov_b32_e32 v239, v167
	global_load_lds_dwordx4 v[186:187], off
	v_lshl_add_u64 v[186:187], s[60:61], 0, v[162:163]
	s_add_i32 m0, s59, 0x2000
	v_lshl_add_u64 v[188:189], s[34:35], 0, v[166:167]
	global_load_lds_dwordx4 v[186:187], off
	s_mov_b32 m0, s39
	v_lshl_add_u64 v[186:187], s[34:35], 0, v[238:239]
	global_load_lds_dwordx4 v166, s[34:35]
	s_mov_b32 m0, s40
	s_nop 0
	global_load_lds_dwordx4 v238, s[34:35]
	s_waitcnt vmcnt(8)
	s_waitcnt lgkmcnt(0)
	s_barrier
	s_setprio 1
	s_waitcnt lgkmcnt(0)
	s_cmp_eq_u32 s101, 0
	s_cbranch_scc1 .Lmy_z_p8_2
	s_nop 1
	v_mfma_f32_16x16x128_f8f6f4 v[94:97], v[18:25], v[204:211], v[94:97]
	v_mfma_f32_16x16x128_f8f6f4 v[86:89], v[26:33], v[204:211], v[86:89]
	v_mfma_f32_16x16x128_f8f6f4 v[78:81], v[18:25], v[212:219], v[78:81]
	v_mfma_f32_16x16x128_f8f6f4 v[66:69], v[26:33], v[212:219], v[66:69]
	v_mfma_f32_16x16x128_f8f6f4 v[54:57], v[18:25], v[220:227], v[54:57]
	v_mfma_f32_16x16x128_f8f6f4 v[46:49], v[26:33], v[220:227], v[46:49]
	v_mfma_f32_16x16x128_f8f6f4 v[38:41], v[18:25], v[230:237], v[38:41]
	v_mfma_f32_16x16x128_f8f6f4 v[34:37], v[26:33], v[230:237], v[34:37]
	s_branch .Lmy_zd_p8_2
.Lmy_z_p8_2:
	s_nop 1
	v_mfma_f32_16x16x128_f8f6f4 v[94:97], v[18:25], v[204:211], 0
	v_mfma_f32_16x16x128_f8f6f4 v[86:89], v[26:33], v[204:211], 0
	v_mfma_f32_16x16x128_f8f6f4 v[78:81], v[18:25], v[212:219], 0
	v_mfma_f32_16x16x128_f8f6f4 v[66:69], v[26:33], v[212:219], 0
	v_mfma_f32_16x16x128_f8f6f4 v[54:57], v[18:25], v[220:227], 0
	v_mfma_f32_16x16x128_f8f6f4 v[46:49], v[26:33], v[220:227], 0
	v_mfma_f32_16x16x128_f8f6f4 v[38:41], v[18:25], v[230:237], 0
	v_mfma_f32_16x16x128_f8f6f4 v[34:37], v[26:33], v[230:237], 0
.Lmy_zd_p8_2:
	s_setprio 0
	s_setprio 1
	s_cmp_eq_u32 s101, 0
	s_cbranch_scc1 .Lmy_z_p8_3
	s_nop 1
	v_mfma_f32_16x16x128_f8f6f4 v[90:93], v[2:9], v[204:211], v[90:93]
	v_mfma_f32_16x16x128_f8f6f4 v[82:85], v[10:17], v[204:211], v[82:85]
	v_mfma_f32_16x16x128_f8f6f4 v[74:77], v[2:9], v[212:219], v[74:77]
	v_mfma_f32_16x16x128_f8f6f4 v[58:61], v[10:17], v[212:219], v[58:61]
	v_mfma_f32_16x16x128_f8f6f4 v[70:73], v[2:9], v[220:227], v[70:73]
	v_mfma_f32_16x16x128_f8f6f4 v[62:65], v[10:17], v[220:227], v[62:65]
	v_mfma_f32_16x16x128_f8f6f4 v[50:53], v[2:9], v[230:237], v[50:53]
	v_mfma_f32_16x16x128_f8f6f4 v[42:45], v[10:17], v[230:237], v[42:45]
	s_branch .Lmy_zd_p8_3
.Lmy_z_p8_3:
	s_nop 1
	v_mfma_f32_16x16x128_f8f6f4 v[90:93], v[2:9], v[204:211], 0
	v_mfma_f32_16x16x128_f8f6f4 v[82:85], v[10:17], v[204:211], 0
	v_mfma_f32_16x16x128_f8f6f4 v[74:77], v[2:9], v[212:219], 0
	v_mfma_f32_16x16x128_f8f6f4 v[58:61], v[10:17], v[212:219], 0
	v_mfma_f32_16x16x128_f8f6f4 v[70:73], v[2:9], v[220:227], 0
	v_mfma_f32_16x16x128_f8f6f4 v[62:65], v[10:17], v[220:227], 0
	v_mfma_f32_16x16x128_f8f6f4 v[50:53], v[2:9], v[230:237], 0
	v_mfma_f32_16x16x128_f8f6f4 v[42:45], v[10:17], v[230:237], 0
.Lmy_zd_p8_3:
	s_mov_b32 s101, 1
	s_setprio 0
	s_barrier
	v_add_u32_e32 v14, s86, v193
	v_add_u32_e32 v30, s87, v193
	ds_read_b128 v[2:5], v14
	ds_read_b128 v[6:9], v14 offset:1024
	ds_read_b128 v[10:13], v14 offset:2048
	ds_read_b128 v[14:17], v14 offset:3072
	ds_read_b128 v[18:21], v30
	ds_read_b128 v[22:25], v30 offset:1024
	ds_read_b128 v[26:29], v30 offset:2048
	ds_read_b128 v[30:33], v30 offset:3072
	s_mov_b32 m0, s41
	ds_read_b128 v[204:207], v197 offset:32768
	ds_read_b128 v[208:211], v197 offset:33792
	ds_read_b128 v[212:215], v197 offset:34816
	ds_read_b128 v[216:219], v197 offset:35840
	ds_read_b128 v[220:223], v197 offset:36864
	ds_read_b128 v[224:227], v197 offset:37888
	ds_read_b128 v[230:233], v197 offset:38912
	ds_read_b128 v[234:237], v197 offset:39936
	global_load_lds_dwordx4 v229, s[34:35]
	s_mov_b32 m0, s42
	s_nop 0
	global_load_lds_dwordx4 v240, s[34:35]
	s_waitcnt vmcnt(8)
	s_waitcnt lgkmcnt(0)
	s_barrier
	s_setprio 1
	s_waitcnt lgkmcnt(0)
	s_nop 1
	v_mfma_f32_16x16x128_f8f6f4 v[158:161], v[2:9], v[204:211], v[158:161]
	v_mfma_f32_16x16x128_f8f6f4 v[150:153], v[10:17], v[204:211], v[150:153]
	v_mfma_f32_16x16x128_f8f6f4 v[142:145], v[2:9], v[212:219], v[142:145]
	v_mfma_f32_16x16x128_f8f6f4 v[134:137], v[10:17], v[212:219], v[134:137]
	v_mfma_f32_16x16x128_f8f6f4 v[126:129], v[2:9], v[220:227], v[126:129]
	v_mfma_f32_16x16x128_f8f6f4 v[118:121], v[10:17], v[220:227], v[118:121]
	v_mfma_f32_16x16x128_f8f6f4 v[110:113], v[2:9], v[230:237], v[110:113]
	v_mfma_f32_16x16x128_f8f6f4 v[102:105], v[10:17], v[230:237], v[102:105]
	s_setprio 0
	s_setprio 1
	s_nop 1
	v_mfma_f32_16x16x128_f8f6f4 v[154:157], v[18:25], v[204:211], v[154:157]
	v_mfma_f32_16x16x128_f8f6f4 v[146:149], v[26:33], v[204:211], v[146:149]
	v_mfma_f32_16x16x128_f8f6f4 v[138:141], v[18:25], v[212:219], v[138:141]
	v_mfma_f32_16x16x128_f8f6f4 v[130:133], v[26:33], v[212:219], v[130:133]
	v_mfma_f32_16x16x128_f8f6f4 v[122:125], v[18:25], v[220:227], v[122:125]
	v_mfma_f32_16x16x128_f8f6f4 v[114:117], v[26:33], v[220:227], v[114:117]
	v_mfma_f32_16x16x128_f8f6f4 v[106:109], v[18:25], v[230:237], v[106:109]
	v_mfma_f32_16x16x128_f8f6f4 v[98:101], v[26:33], v[230:237], v[98:101]
	s_setprio 0
	s_barrier
	s_add_i32 s34, s86, s38
	v_lshl_add_u64 v[182:183], v[182:183], 0, s[8:9]
	s_mov_b32 m0, s34
	ds_read_b128 v[204:207], v197 offset:49152
	ds_read_b128 v[208:211], v197 offset:50176
	ds_read_b128 v[212:215], v197 offset:51200
	ds_read_b128 v[216:219], v197 offset:52224
	ds_read_b128 v[220:223], v197 offset:53248
	ds_read_b128 v[224:227], v197 offset:54272
	ds_read_b128 v[230:233], v197 offset:55296
	ds_read_b128 v[234:237], v197 offset:56320
	global_load_lds_dwordx4 v[182:183], off
	s_add_i32 m0, s34, 0x2000
	s_add_u32 s30, s30, 0x40080
	v_lshl_add_u64 v[182:183], v[184:185], 0, s[8:9]
	s_addc_u32 s31, s31, 0
	s_add_i32 s34, s87, s38
	global_load_lds_dwordx4 v[182:183], off
	v_lshl_add_u64 v[182:183], s[30:31], 0, v[164:165]
	s_mov_b32 m0, s34
	s_nop 0
	global_load_lds_dwordx4 v[182:183], off
	v_lshl_add_u64 v[182:183], s[30:31], 0, v[162:163]
	s_add_i32 m0, s34, 0x2000
	s_nop 0
	global_load_lds_dwordx4 v[182:183], off
	v_lshl_add_u64 v[182:183], v[188:189], 0, s[8:9]
	s_mov_b32 m0, s43
	s_nop 0
	global_load_lds_dwordx4 v[182:183], off
	v_lshl_add_u64 v[182:183], v[186:187], 0, s[8:9]
	s_mov_b32 m0, s44
	s_nop 0
	global_load_lds_dwordx4 v[182:183], off
	s_waitcnt vmcnt(8)
	s_waitcnt lgkmcnt(0)
	s_barrier
	s_setprio 1
	s_waitcnt lgkmcnt(0)
	s_nop 1
	v_mfma_f32_16x16x128_f8f6f4 v[94:97], v[2:9], v[204:211], v[94:97]
	v_mfma_f32_16x16x128_f8f6f4 v[86:89], v[10:17], v[204:211], v[86:89]
	v_mfma_f32_16x16x128_f8f6f4 v[78:81], v[2:9], v[212:219], v[78:81]
	v_mfma_f32_16x16x128_f8f6f4 v[66:69], v[10:17], v[212:219], v[66:69]
	v_mfma_f32_16x16x128_f8f6f4 v[54:57], v[2:9], v[220:227], v[54:57]
	v_mfma_f32_16x16x128_f8f6f4 v[46:49], v[10:17], v[220:227], v[46:49]
	v_mfma_f32_16x16x128_f8f6f4 v[38:41], v[2:9], v[230:237], v[38:41]
	v_mfma_f32_16x16x128_f8f6f4 v[34:37], v[10:17], v[230:237], v[34:37]
	s_setprio 0
	s_setprio 1
	s_nop 1
	v_mfma_f32_16x16x128_f8f6f4 v[90:93], v[18:25], v[204:211], v[90:93]
	v_mfma_f32_16x16x128_f8f6f4 v[82:85], v[26:33], v[204:211], v[82:85]
	v_mfma_f32_16x16x128_f8f6f4 v[74:77], v[18:25], v[212:219], v[74:77]
	v_mfma_f32_16x16x128_f8f6f4 v[58:61], v[26:33], v[212:219], v[58:61]
	v_mfma_f32_16x16x128_f8f6f4 v[70:73], v[18:25], v[220:227], v[70:73]
	v_mfma_f32_16x16x128_f8f6f4 v[62:65], v[26:33], v[220:227], v[62:65]
	v_mfma_f32_16x16x128_f8f6f4 v[50:53], v[18:25], v[230:237], v[50:53]
	v_mfma_f32_16x16x128_f8f6f4 v[42:45], v[26:33], v[230:237], v[42:45]
	s_setprio 0
	s_barrier
	s_add_i32 s58, s58, 2
	s_add_u32 s26, s26, 0x100
	s_addc_u32 s27, s27, 0
	s_cmp_gt_u32 s58, 13
	s_cbranch_scc1 .LBB0_1350

.LBB0_1418:
	s_add_u32 s26, s26, 0x80
	s_addc_u32 s27, s27, 0
	s_add_u32 s34, s30, 0x100
	s_mov_b32 s101, 0
	s_addc_u32 s35, s31, 0
	s_mov_b32 s50, -2
.LBB0_1419:
	ds_read_b128 v[18:21], v192
	ds_read_b128 v[22:25], v192 offset:1024
	ds_read_b128 v[26:29], v192 offset:2048
	ds_read_b128 v[30:33], v192 offset:3072
	ds_read_b128 v[2:5], v193
	ds_read_b128 v[6:9], v193 offset:1024
	ds_read_b128 v[10:13], v193 offset:2048
	ds_read_b128 v[14:17], v193 offset:3072
	s_add_u32 s28, s26, 0x80
	s_addc_u32 s29, s27, 0
	s_cmp_eq_u32 s50, 12
	s_cselect_b32 s31, s19, s29
	s_cselect_b32 s30, s18, s28
	s_cselect_b32 s29, s21, s35
	s_cselect_b32 s28, s20, s34
	v_lshl_add_u64 v[220:221], s[26:27], 0, v[178:179]
	s_add_i32 m0, s38, 0xc000
	ds_read_b128 v[180:183], v194
	ds_read_b128 v[184:187], v194 offset:1024
	ds_read_b128 v[196:199], v194 offset:2048
	ds_read_b128 v[200:203], v194 offset:3072
	ds_read_b128 v[204:207], v194 offset:4096
	ds_read_b128 v[208:211], v194 offset:5120
	ds_read_b128 v[212:215], v194 offset:6144
	ds_read_b128 v[216:219], v194 offset:7168
	global_load_lds_dwordx4 v[220:221], off
	v_lshl_add_u64 v[220:221], s[26:27], 0, v[176:177]
	s_add_i32 m0, s38, 0xe000
	s_nop 0
	global_load_lds_dwordx4 v[220:221], off
	s_waitcnt vmcnt(8)
	s_waitcnt lgkmcnt(0)
	s_barrier
	s_setprio 1
	s_waitcnt lgkmcnt(0)
	s_cmp_eq_u32 s101, 0
	s_cbranch_scc1 .Lmy_z_p9_0
	s_nop 1
	v_mfma_f32_16x16x128_f8f6f4 v[158:161], v[18:25], v[180:187], v[158:161]
	v_mfma_f32_16x16x128_f8f6f4 v[154:157], v[26:33], v[180:187], v[154:157]
	v_mfma_f32_16x16x128_f8f6f4 v[142:145], v[18:25], v[196:203], v[142:145]
	v_mfma_f32_16x16x128_f8f6f4 v[138:141], v[26:33], v[196:203], v[138:141]
	v_mfma_f32_16x16x128_f8f6f4 v[126:129], v[18:25], v[204:211], v[126:129]
	v_mfma_f32_16x16x128_f8f6f4 v[122:125], v[26:33], v[204:211], v[122:125]
	v_mfma_f32_16x16x128_f8f6f4 v[110:113], v[18:25], v[212:219], v[110:113]
	v_mfma_f32_16x16x128_f8f6f4 v[106:109], v[26:33], v[212:219], v[106:109]
	s_branch .Lmy_zd_p9_0
.Lmy_z_p9_0:
	s_nop 1
	v_mfma_f32_16x16x128_f8f6f4 v[158:161], v[18:25], v[180:187], 0
	v_mfma_f32_16x16x128_f8f6f4 v[154:157], v[26:33], v[180:187], 0
	v_mfma_f32_16x16x128_f8f6f4 v[142:145], v[18:25], v[196:203], 0
	v_mfma_f32_16x16x128_f8f6f4 v[138:141], v[26:33], v[196:203], 0
	v_mfma_f32_16x16x128_f8f6f4 v[126:129], v[18:25], v[204:211], 0
	v_mfma_f32_16x16x128_f8f6f4 v[122:125], v[26:33], v[204:211], 0
	v_mfma_f32_16x16x128_f8f6f4 v[110:113], v[18:25], v[212:219], 0
	v_mfma_f32_16x16x128_f8f6f4 v[106:109], v[26:33], v[212:219], 0
.Lmy_zd_p9_0:
	s_setprio 0
	s_setprio 1
	s_cmp_eq_u32 s101, 0
	s_cbranch_scc1 .Lmy_z_p9_1
	s_nop 1
	v_mfma_f32_16x16x128_f8f6f4 v[150:153], v[2:9], v[180:187], v[150:153]
	v_mfma_f32_16x16x128_f8f6f4 v[146:149], v[10:17], v[180:187], v[146:149]
	v_mfma_f32_16x16x128_f8f6f4 v[134:137], v[2:9], v[196:203], v[134:137]
	v_mfma_f32_16x16x128_f8f6f4 v[130:133], v[10:17], v[196:203], v[130:133]
	v_mfma_f32_16x16x128_f8f6f4 v[118:121], v[2:9], v[204:211], v[118:121]
	v_mfma_f32_16x16x128_f8f6f4 v[114:117], v[10:17], v[204:211], v[114:117]
	v_mfma_f32_16x16x128_f8f6f4 v[94:97], v[2:9], v[212:219], v[94:97]
	v_mfma_f32_16x16x128_f8f6f4 v[90:93], v[10:17], v[212:219], v[90:93]
	s_branch .Lmy_zd_p9_1
.Lmy_z_p9_1:
	s_nop 1
	v_mfma_f32_16x16x128_f8f6f4 v[150:153], v[2:9], v[180:187], 0
	v_mfma_f32_16x16x128_f8f6f4 v[146:149], v[10:17], v[180:187], 0
	v_mfma_f32_16x16x128_f8f6f4 v[134:137], v[2:9], v[196:203], 0
	v_mfma_f32_16x16x128_f8f6f4 v[130:133], v[10:17], v[196:203], 0
	v_mfma_f32_16x16x128_f8f6f4 v[118:121], v[2:9], v[204:211], 0
	v_mfma_f32_16x16x128_f8f6f4 v[114:117], v[10:17], v[204:211], 0
	v_mfma_f32_16x16x128_f8f6f4 v[94:97], v[2:9], v[212:219], 0
	v_mfma_f32_16x16x128_f8f6f4 v[90:93], v[10:17], v[212:219], 0
.Lmy_zd_p9_1:
	s_setprio 0
	s_barrier
	s_add_i32 s51, s3, s37
	v_lshl_add_u64 v[180:181], s[28:29], 0, v[164:165]
	s_mov_b32 m0, s51
	ds_read_b128 v[196:199], v194 offset:16384
	ds_read_b128 v[200:203], v194 offset:17408
	ds_read_b128 v[204:207], v194 offset:18432
	ds_read_b128 v[208:211], v194 offset:19456
	ds_read_b128 v[212:215], v194 offset:20480
	ds_read_b128 v[216:219], v194 offset:21504
	ds_read_b128 v[220:223], v194 offset:22528
	ds_read_b128 v[224:227], v194 offset:23552
	global_load_lds_dwordx4 v[180:181], off
	s_add_i32 m0, s51, 0x2000
	s_add_u32 s52, s28, 0x40000
	v_lshl_add_u64 v[182:183], s[28:29], 0, v[162:163]
	s_addc_u32 s53, s29, 0
	s_add_i32 s51, s2, s37
	global_load_lds_dwordx4 v[182:183], off
	v_lshl_add_u64 v[184:185], s[52:53], 0, v[164:165]
	s_mov_b32 m0, s51
	v_lshl_add_u64 v[186:187], s[30:31], 0, v[168:169]
	global_load_lds_dwordx4 v[184:185], off
	v_lshl_add_u64 v[184:185], s[52:53], 0, v[162:163]
	s_add_i32 m0, s51, 0x2000
	s_nop 0
	global_load_lds_dwordx4 v[184:185], off
	v_lshl_add_u64 v[184:185], s[30:31], 0, v[166:167]
	s_mov_b32 m0, s38
	s_nop 0
	global_load_lds_dwordx4 v[184:185], off
	s_mov_b32 m0, s39
	s_nop 0
	global_load_lds_dwordx4 v[186:187], off
	s_waitcnt vmcnt(8)
	s_waitcnt lgkmcnt(0)
	s_barrier
	s_setprio 1
	s_waitcnt lgkmcnt(0)
	s_cmp_eq_u32 s101, 0
	s_cbranch_scc1 .Lmy_z_p9_2
	s_nop 1
	v_mfma_f32_16x16x128_f8f6f4 v[78:81], v[18:25], v[196:203], v[78:81]
	v_mfma_f32_16x16x128_f8f6f4 v[74:77], v[26:33], v[196:203], v[74:77]
	v_mfma_f32_16x16x128_f8f6f4 v[62:65], v[18:25], v[204:211], v[62:65]
	v_mfma_f32_16x16x128_f8f6f4 v[58:61], v[26:33], v[204:211], v[58:61]
	v_mfma_f32_16x16x128_f8f6f4 v[46:49], v[18:25], v[212:219], v[46:49]
	v_mfma_f32_16x16x128_f8f6f4 v[42:45], v[26:33], v[212:219], v[42:45]
	v_mfma_f32_16x16x128_f8f6f4 v[38:41], v[18:25], v[220:227], v[38:41]
	v_mfma_f32_16x16x128_f8f6f4 v[34:37], v[26:33], v[220:227], v[34:37]
	s_branch .Lmy_zd_p9_2
.Lmy_z_p9_2:
	s_nop 1
	v_mfma_f32_16x16x128_f8f6f4 v[78:81], v[18:25], v[196:203], 0
	v_mfma_f32_16x16x128_f8f6f4 v[74:77], v[26:33], v[196:203], 0
	v_mfma_f32_16x16x128_f8f6f4 v[62:65], v[18:25], v[204:211], 0
	v_mfma_f32_16x16x128_f8f6f4 v[58:61], v[26:33], v[204:211], 0
	v_mfma_f32_16x16x128_f8f6f4 v[46:49], v[18:25], v[212:219], 0
	v_mfma_f32_16x16x128_f8f6f4 v[42:45], v[26:33], v[212:219], 0
	v_mfma_f32_16x16x128_f8f6f4 v[38:41], v[18:25], v[220:227], 0
	v_mfma_f32_16x16x128_f8f6f4 v[34:37], v[26:33], v[220:227], 0
.Lmy_zd_p9_2:
	s_setprio 0
	s_setprio 1
	s_cmp_eq_u32 s101, 0
	s_cbranch_scc1 .Lmy_z_p9_3
	s_nop 1
	v_mfma_f32_16x16x128_f8f6f4 v[98:101], v[2:9], v[196:203], v[98:101]
	v_mfma_f32_16x16x128_f8f6f4 v[102:105], v[10:17], v[196:203], v[102:105]
	v_mfma_f32_16x16x128_f8f6f4 v[82:85], v[2:9], v[204:211], v[82:85]
	v_mfma_f32_16x16x128_f8f6f4 v[86:89], v[10:17], v[204:211], v[86:89]
	v_mfma_f32_16x16x128_f8f6f4 v[66:69], v[2:9], v[212:219], v[66:69]
	v_mfma_f32_16x16x128_f8f6f4 v[70:73], v[10:17], v[212:219], v[70:73]
	v_mfma_f32_16x16x128_f8f6f4 v[50:53], v[2:9], v[220:227], v[50:53]
	v_mfma_f32_16x16x128_f8f6f4 v[54:57], v[10:17], v[220:227], v[54:57]
	s_branch .Lmy_zd_p9_3
.Lmy_z_p9_3:
	s_nop 1
	v_mfma_f32_16x16x128_f8f6f4 v[98:101], v[2:9], v[196:203], 0
	v_mfma_f32_16x16x128_f8f6f4 v[102:105], v[10:17], v[196:203], 0
	v_mfma_f32_16x16x128_f8f6f4 v[82:85], v[2:9], v[204:211], 0
	v_mfma_f32_16x16x128_f8f6f4 v[86:89], v[10:17], v[204:211], 0
	v_mfma_f32_16x16x128_f8f6f4 v[66:69], v[2:9], v[212:219], 0
	v_mfma_f32_16x16x128_f8f6f4 v[70:73], v[10:17], v[212:219], 0
	v_mfma_f32_16x16x128_f8f6f4 v[50:53], v[2:9], v[220:227], 0
	v_mfma_f32_16x16x128_f8f6f4 v[54:57], v[10:17], v[220:227], 0
.Lmy_zd_p9_3:
	s_mov_b32 s101, 1
	s_setprio 0
	s_barrier
	v_add_u32_e32 v14, s86, v188
	v_add_u32_e32 v30, s87, v188
	ds_read_b128 v[2:5], v14
	ds_read_b128 v[6:9], v14 offset:1024
	ds_read_b128 v[10:13], v14 offset:2048
	ds_read_b128 v[14:17], v14 offset:3072
	ds_read_b128 v[18:21], v30
	ds_read_b128 v[22:25], v30 offset:1024
	ds_read_b128 v[26:29], v30 offset:2048
	ds_read_b128 v[30:33], v30 offset:3072
	s_mov_b32 m0, s40
	v_lshl_add_u64 v[230:231], s[30:31], 0, v[170:171]
	ds_read_b128 v[196:199], v194 offset:32768
	ds_read_b128 v[200:203], v194 offset:33792
	ds_read_b128 v[204:207], v194 offset:34816
	ds_read_b128 v[208:211], v194 offset:35840
	ds_read_b128 v[212:215], v194 offset:36864
	ds_read_b128 v[216:219], v194 offset:37888
	ds_read_b128 v[220:223], v194 offset:38912
	ds_read_b128 v[224:227], v194 offset:39936
	global_load_lds_dwordx4 v[230:231], off
	v_lshl_add_u64 v[230:231], s[30:31], 0, v[172:173]
	s_mov_b32 m0, s41
	s_nop 0
	global_load_lds_dwordx4 v[230:231], off
	s_waitcnt vmcnt(8)
	s_waitcnt lgkmcnt(0)
	s_barrier
	s_setprio 1
	s_waitcnt lgkmcnt(0)
	s_nop 1
	v_mfma_f32_16x16x128_f8f6f4 v[158:161], v[2:9], v[196:203], v[158:161]
	v_mfma_f32_16x16x128_f8f6f4 v[154:157], v[10:17], v[196:203], v[154:157]
	v_mfma_f32_16x16x128_f8f6f4 v[142:145], v[2:9], v[204:211], v[142:145]
	v_mfma_f32_16x16x128_f8f6f4 v[138:141], v[10:17], v[204:211], v[138:141]
	v_mfma_f32_16x16x128_f8f6f4 v[126:129], v[2:9], v[212:219], v[126:129]
	v_mfma_f32_16x16x128_f8f6f4 v[122:125], v[10:17], v[212:219], v[122:125]
	v_mfma_f32_16x16x128_f8f6f4 v[110:113], v[2:9], v[220:227], v[110:113]
	v_mfma_f32_16x16x128_f8f6f4 v[106:109], v[10:17], v[220:227], v[106:109]
	s_setprio 0
	s_setprio 1
	s_nop 1
	v_mfma_f32_16x16x128_f8f6f4 v[150:153], v[18:25], v[196:203], v[150:153]
	v_mfma_f32_16x16x128_f8f6f4 v[146:149], v[26:33], v[196:203], v[146:149]
	v_mfma_f32_16x16x128_f8f6f4 v[134:137], v[18:25], v[204:211], v[134:137]
	v_mfma_f32_16x16x128_f8f6f4 v[130:133], v[26:33], v[204:211], v[130:133]
	v_mfma_f32_16x16x128_f8f6f4 v[118:121], v[18:25], v[212:219], v[118:121]
	v_mfma_f32_16x16x128_f8f6f4 v[114:117], v[26:33], v[212:219], v[114:117]
	v_mfma_f32_16x16x128_f8f6f4 v[94:97], v[18:25], v[220:227], v[94:97]
	v_mfma_f32_16x16x128_f8f6f4 v[90:93], v[26:33], v[220:227], v[90:93]
	s_setprio 0
	s_barrier
	s_add_i32 s30, s86, s37
	v_lshl_add_u64 v[180:181], v[180:181], 0, s[8:9]
	s_mov_b32 m0, s30
	ds_read_b128 v[196:199], v194 offset:49152
	ds_read_b128 v[200:203], v194 offset:50176
	ds_read_b128 v[204:207], v194 offset:51200
	ds_read_b128 v[208:211], v194 offset:52224
	ds_read_b128 v[212:215], v194 offset:53248
	ds_read_b128 v[216:219], v194 offset:54272
	ds_read_b128 v[220:223], v194 offset:55296
	ds_read_b128 v[224:227], v194 offset:56320
	global_load_lds_dwordx4 v[180:181], off
	s_add_i32 m0, s30, 0x2000
	s_add_u32 s28, s28, 0x40080
	v_lshl_add_u64 v[180:181], v[182:183], 0, s[8:9]
	s_addc_u32 s29, s29, 0
	s_add_i32 s30, s87, s37
	global_load_lds_dwordx4 v[180:181], off
	v_lshl_add_u64 v[180:181], s[28:29], 0, v[164:165]
	s_mov_b32 m0, s30
	s_nop 0
	global_load_lds_dwordx4 v[180:181], off
	v_lshl_add_u64 v[180:181], s[28:29], 0, v[162:163]
	s_add_i32 m0, s30, 0x2000
	s_nop 0
	global_load_lds_dwordx4 v[180:181], off
	v_lshl_add_u64 v[180:181], v[184:185], 0, s[8:9]
	s_mov_b32 m0, s43
	s_nop 0
	global_load_lds_dwordx4 v[180:181], off
	v_lshl_add_u64 v[180:181], v[186:187], 0, s[8:9]
	s_mov_b32 m0, s44
	s_nop 0
	global_load_lds_dwordx4 v[180:181], off
	s_waitcnt vmcnt(8)
	s_waitcnt lgkmcnt(0)
	s_barrier
	s_setprio 1
	s_waitcnt lgkmcnt(0)
	s_nop 1
	v_mfma_f32_16x16x128_f8f6f4 v[78:81], v[2:9], v[196:203], v[78:81]
	v_mfma_f32_16x16x128_f8f6f4 v[74:77], v[10:17], v[196:203], v[74:77]
	v_mfma_f32_16x16x128_f8f6f4 v[62:65], v[2:9], v[204:211], v[62:65]
	v_mfma_f32_16x16x128_f8f6f4 v[58:61], v[10:17], v[204:211], v[58:61]
	v_mfma_f32_16x16x128_f8f6f4 v[46:49], v[2:9], v[212:219], v[46:49]
	v_mfma_f32_16x16x128_f8f6f4 v[42:45], v[10:17], v[212:219], v[42:45]
	v_mfma_f32_16x16x128_f8f6f4 v[38:41], v[2:9], v[220:227], v[38:41]
	v_mfma_f32_16x16x128_f8f6f4 v[34:37], v[10:17], v[220:227], v[34:37]
	s_setprio 0
	s_setprio 1
	s_nop 1
	v_mfma_f32_16x16x128_f8f6f4 v[98:101], v[18:25], v[196:203], v[98:101]
	v_mfma_f32_16x16x128_f8f6f4 v[102:105], v[26:33], v[196:203], v[102:105]
	v_mfma_f32_16x16x128_f8f6f4 v[82:85], v[18:25], v[204:211], v[82:85]
	v_mfma_f32_16x16x128_f8f6f4 v[86:89], v[26:33], v[204:211], v[86:89]
	v_mfma_f32_16x16x128_f8f6f4 v[66:69], v[18:25], v[212:219], v[66:69]
	v_mfma_f32_16x16x128_f8f6f4 v[70:73], v[26:33], v[212:219], v[70:73]
	v_mfma_f32_16x16x128_f8f6f4 v[50:53], v[18:25], v[220:227], v[50:53]
	v_mfma_f32_16x16x128_f8f6f4 v[54:57], v[26:33], v[220:227], v[54:57]
	s_setprio 0
	s_barrier
	s_add_i32 s50, s50, 2
	s_add_u32 s26, s26, 0x100
	s_addc_u32 s27, s27, 0
	s_add_u32 s34, s34, 0x100
	s_addc_u32 s35, s35, 0
	s_cmp_gt_u32 s50, 13
	s_cbranch_scc0 .LBB0_1419
	s_and_b64 vcc, exec, s[14:15]
	s_cbranch_vccz .LBB0_1422
	s_barrier
